# v85: M3 retention epilogue gate rows and norm weights requested right after the item barrier (into otherwise unused registers) instead of behind the last state MFMA
# speedup vs baseline: 1.0074x; 1.0070x over previous
.LBB0_555:
	s_and_b32 s33, s3, 1
	s_lshl_b32 s4, s33, 1
	s_add_i32 s14, s4, s18
	s_mul_i32 s4, s10, 0x1100
	s_lshl_b32 s5, s11, 7
	s_add_i32 s45, s4, s5
	s_lshl_b32 s22, s14, 6
	v_or_b32_e32 v2, s45, v116
	v_mov_b64_e32 v[50:51], s[88:89]
	s_mul_i32 s5, s14, 0x44
	s_ashr_i32 s23, s22, 31
	v_mad_i64_i32 v[2:3], s[14:15], v2, s60, v[50:51]
	s_lshl_b64 s[14:15], s[22:23], 1
	v_mov_b32_e32 v101, v0
	v_lshl_add_u64 v[2:3], v[2:3], 0, s[14:15]
	v_or_b32_e32 v10, s45, v117
	v_lshl_add_u64 v[2:3], v[2:3], 0, v[100:101]
	v_mad_i64_i32 v[10:11], s[26:27], v10, s60, v[50:51]
	s_mul_i32 s4, s10, 0x110
	v_add_co_u32_e32 v6, vcc, s78, v2
	v_lshl_add_u64 v[10:11], v[10:11], 0, s[14:15]
	v_or_b32_e32 v18, s45, v118
	s_add_i32 s4, s4, s5
	v_addc_co_u32_e32 v7, vcc, 0, v3, vcc
	v_lshl_add_u64 v[10:11], v[10:11], 0, v[100:101]
	v_mad_i64_i32 v[18:19], s[26:27], v18, s60, v[50:51]
	s_add_i32 s4, s4, s11
	v_add_co_u32_e32 v14, vcc, s78, v10
	v_lshl_add_u64 v[18:19], v[18:19], 0, s[14:15]
	v_or_b32_e32 v26, s45, v119
	s_ashr_i32 s5, s4, 31
	v_addc_co_u32_e32 v15, vcc, 0, v11, vcc
	v_lshl_add_u64 v[18:19], v[18:19], 0, v[100:101]
	v_mad_i64_i32 v[26:27], s[26:27], v26, s60, v[50:51]
	s_lshl_b64 s[10:11], s[4:5], 13
	s_add_i32 s4, s4, 34
	v_add_co_u32_e32 v22, vcc, s78, v18
	v_lshl_add_u64 v[26:27], v[26:27], 0, s[14:15]
	s_ashr_i32 s5, s4, 31
	v_addc_co_u32_e32 v23, vcc, 0, v19, vcc
	v_lshl_add_u64 v[26:27], v[26:27], 0, v[100:101]
	s_lshl_b64 s[4:5], s[4:5], 13
	v_add_co_u32_e32 v30, vcc, s78, v26
	s_cmp_eq_u32 s33, 0
	s_nop 0
	v_addc_co_u32_e32 v31, vcc, 0, v27, vcc
	s_cselect_b64 vcc, -1, 0
	s_add_u32 s10, s66, s10
	s_addc_u32 s11, s67, s11
	s_add_u32 s4, s66, s4
	s_addc_u32 s5, s67, s5
	v_or_b32_e32 v104, s45, v109
	global_load_dwordx4 v[2:5], v[6:7], off offset:512
	s_nop 0
	global_load_dwordx4 v[6:9], v[6:7], off
	s_nop 0
	global_load_dwordx4 v[10:13], v[14:15], off offset:512
	s_nop 0
	global_load_dwordx4 v[14:17], v[14:15], off
	s_nop 0
	global_load_dwordx4 v[18:21], v[22:23], off offset:512
	s_nop 0
	global_load_dwordx4 v[22:25], v[22:23], off
	s_nop 0
	global_load_dwordx4 v[26:29], v[30:31], off offset:512
	s_nop 0
	global_load_dwordx4 v[30:33], v[30:31], off
	s_nop 0
	global_load_dwordx4 v[34:37], v125, s[10:11]
	global_load_dwordx4 v[38:41], v125, s[4:5]
	global_load_dwordx4 v[42:45], v126, s[10:11]
	global_load_dwordx4 v[46:49], v126, s[4:5]
	v_mad_i64_i32 v[106:107], s[4:5], v104, s60, v[50:51]
	v_lshl_add_u64 v[50:51], v[106:107], 0, s[14:15]
	v_mov_b32_e32 v103, v0
	v_lshl_add_u64 v[50:51], v[50:51], 0, v[102:103]
	global_load_dwordx4 v[78:81], v[50:51], off offset:3584
	global_load_dwordx4 v[74:77], v[50:51], off offset:3616
	global_load_dwordx4 v[70:73], v[50:51], off offset:3648
	global_load_dwordx4 v[66:69], v[50:51], off offset:3680
	v_cndmask_b32_e32 v50, v142, v1, vcc
	s_mov_b32 s10, 0
	v_mul_f32_e32 v101, 0xbfb8aa3b, v50
	v_ashrrev_i32_e32 v105, 31, v104
	s_mov_b64 s[4:5], -1
	s_waitcnt vmcnt(15)
	ds_write_b128 v127, v[2:5]
	s_waitcnt vmcnt(14)
	ds_write_b128 v128, v[6:9] offset:16384
	s_waitcnt vmcnt(13)
	ds_write_b128 v129, v[10:13]
	s_waitcnt vmcnt(12)
	ds_write_b128 v130, v[14:17] offset:16384
	s_waitcnt vmcnt(11)
	ds_write_b128 v127, v[18:21] offset:8192
	s_waitcnt vmcnt(10)
	ds_write_b128 v131, v[22:25] offset:16384
	s_waitcnt vmcnt(9)
	ds_write_b128 v132, v[26:29] offset:8192
	s_waitcnt vmcnt(8)
	ds_write_b128 v133, v[30:33] offset:16384
	s_waitcnt vmcnt(7)
	ds_write_b128 v128, v[34:37] offset:32768
	s_waitcnt vmcnt(6)
	ds_write_b128 v128, v[38:41] offset:40960
	s_waitcnt vmcnt(5)
	ds_write_b128 v130, v[42:45] offset:32768
	s_waitcnt vmcnt(4)
	ds_write_b128 v130, v[46:49] offset:40960
	v_cndmask_b32_e32 v2, v143, v141, vcc
	v_mov_b32_e32 v18, 0
	v_mul_f32_e32 v103, 0xbfb8aa3b, v2
	v_mul_f32_e32 v167, 0xbf800000, v101
	v_mul_f32_e32 v168, 0xc0000000, v101
	v_mul_f32_e32 v169, 0xc0400000, v101
	v_mul_f32_e32 v170, 0xc1000000, v101
	v_mul_f32_e32 v171, 0x3f800000, v103
	v_mul_f32_e32 v172, 0x40000000, v103
	v_mul_f32_e32 v173, 0x40400000, v103
	v_mul_f32_e32 v174, 0x41000000, v103
	v_exp_f32_e32 v167, v167
	v_exp_f32_e32 v168, v168
	v_exp_f32_e32 v169, v169
	v_exp_f32_e32 v170, v170
	v_exp_f32_e32 v171, v171
	v_exp_f32_e32 v172, v172
	v_exp_f32_e32 v173, v173
	v_exp_f32_e32 v174, v174
	v_mov_b32_e32 v19, v18
	v_mov_b32_e32 v20, v18
	v_mov_b32_e32 v21, v18
	v_mov_b32_e32 v22, v18
	v_mov_b32_e32 v23, v18
	v_mov_b32_e32 v24, v18
	v_mov_b32_e32 v25, v18
	v_mov_b32_e32 v26, v18
	v_mov_b32_e32 v27, v18
	v_mov_b32_e32 v28, v18
	v_mov_b32_e32 v29, v18
	v_mov_b32_e32 v30, v18
	v_mov_b32_e32 v31, v18
	v_mov_b32_e32 v32, v18
	v_mov_b32_e32 v33, v18
	v_mov_b32_e32 v2, v18
	v_mov_b32_e32 v3, v18
	v_mov_b32_e32 v4, v18
	v_mov_b32_e32 v5, v18
	v_mov_b32_e32 v6, v18
	v_mov_b32_e32 v7, v18
	v_mov_b32_e32 v8, v18
	v_mov_b32_e32 v9, v18
	v_mov_b32_e32 v10, v18
	v_mov_b32_e32 v11, v18
	v_mov_b32_e32 v12, v18
	v_mov_b32_e32 v13, v18
	v_mov_b32_e32 v14, v18
	v_mov_b32_e32 v15, v18
	v_mov_b32_e32 v16, v18
	v_mov_b32_e32 v17, v18
	s_waitcnt lgkmcnt(0)
	s_barrier
	v_lshl_add_u64 v[152:153], s[22:23], 1, v[106:107]
	v_lshlrev_b32_e32 v154, 1, v82
	v_mov_b32_e32 v155, v0
	v_lshl_add_u64 v[152:153], v[152:153], 0, v[154:155]
	s_mov_b64 s[98:99], 0x1400
	ds_read_b64 v[156:157], v0 offset:640
	v_lshl_add_u64 v[154:155], v[152:153], 0, s[98:99]
	v_add_co_u32_e32 v152, vcc, s78, v152
	s_lshl_b64 s[98:99], s[24:25], 2
	s_lshl_b64 s[100:101], s[22:23], 2
	v_addc_co_u32_e32 v153, vcc, 0, v153, vcc
	global_load_dwordx2 v[222:223], v[152:153], off offset:1024
	global_load_dwordx2 v[224:225], v[154:155], off offset:16
	global_load_dwordx2 v[226:227], v[154:155], off offset:32
	global_load_dwordx2 v[228:229], v[154:155], off offset:48
	global_load_dwordx2 v[230:231], v[154:155], off offset:64
	global_load_dwordx2 v[232:233], v[154:155], off offset:80
	global_load_dwordx2 v[234:235], v[154:155], off offset:96
	global_load_dwordx2 v[236:237], v[154:155], off offset:112
	s_add_u32 s98, s98, s100
	s_addc_u32 s99, s99, s101
	s_waitcnt lgkmcnt(0)
	v_readfirstlane_b32 s100, v156
	v_readfirstlane_b32 s101, v157
	v_lshlrev_b32_e32 v152, 2, v82
	s_add_u32 s98, s100, s98
	s_addc_u32 s99, s101, s99
	global_load_dwordx4 v[238:241], v152, s[98:99]
	global_load_dwordx4 v[242:245], v152, s[98:99] offset:32
	global_load_dwordx4 v[246:249], v152, s[98:99] offset:64
	global_load_dwordx4 v[250:253], v152, s[98:99] offset:96
	global_load_dwordx4 v[200:203], v152, s[98:99] offset:128
	global_load_dwordx4 v[204:207], v152, s[98:99] offset:160
	global_load_dwordx4 v[214:217], v152, s[98:99] offset:192
	global_load_dwordx4 v[192:195], v152, s[98:99] offset:224
.LBB0_556:
	v_cndmask_b32_e64 v34, 0, 1, s[4:5]
	s_lshl_b32 s4, s10, 6
	v_cmp_ne_u32_e32 vcc, 1, v34
	v_or_b32_e32 v34, s4, v108
	v_lshl_add_u32 v152, v34, 7, s58
	v_add_u32_e32 v38, v152, v120
	ds_read_b128 v[34:37], v38 offset:16384
	ds_read_b128 v[50:53], v38 offset:20480
	v_add_u32_e32 v148, v152, v121
	s_waitcnt vmcnt(19) lgkmcnt(1)
	v_mfma_f32_32x32x16_bf16 v[34:49], v[34:37], v[78:81], 0
	ds_read_b128 v[144:147], v148 offset:16384
	ds_read_b128 v[148:151], v148 offset:20480
	s_waitcnt lgkmcnt(2)
	v_mfma_f32_32x32x16_bf16 v[50:65], v[50:53], v[78:81], 0
	s_waitcnt vmcnt(18) lgkmcnt(1)
	v_mfma_f32_32x32x16_bf16 v[34:49], v[144:147], v[74:77], v[34:49]
	s_waitcnt lgkmcnt(0)
	v_mfma_f32_32x32x16_bf16 v[50:65], v[148:151], v[74:77], v[50:65]
	v_add_u32_e32 v148, v152, v122
	ds_read_b128 v[144:147], v148 offset:16384
	ds_read_b128 v[148:151], v148 offset:20480
	s_waitcnt vmcnt(17) lgkmcnt(1)
	v_mfma_f32_32x32x16_bf16 v[34:49], v[144:147], v[70:73], v[34:49]
	s_waitcnt lgkmcnt(0)
	v_mfma_f32_32x32x16_bf16 v[50:65], v[148:151], v[70:73], v[50:65]
	v_add_u32_e32 v148, v152, v123
	ds_read_b128 v[144:147], v148 offset:16384
	ds_read_b128 v[148:151], v148 offset:20480
	s_waitcnt vmcnt(16) lgkmcnt(1)
	v_mfma_f32_32x32x16_bf16 v[34:49], v[144:147], v[66:69], v[34:49]
	v_or_b32_e32 v145, s4, v82
	s_waitcnt lgkmcnt(0)
	v_mfma_f32_32x32x16_bf16 v[50:65], v[148:151], v[66:69], v[50:65]
	v_sub_u32_e32 v166, v109, v145
	v_cvt_f32_i32_e32 v166, v166
	v_mul_f32_e32 v175, v101, v166
	v_mul_f32_e64 v183, -v103, v166
	v_exp_f32_e32 v175, v175
	v_exp_f32_e32 v183, v183
	s_nop 0
	v_mul_f32_e32 v176, v175, v170
	v_mul_f32_e32 v184, v183, v174
	v_mul_f32_e32 v177, v176, v170
	v_mul_f32_e32 v185, v184, v174
	v_mul_f32_e32 v178, v177, v170
	v_mul_f32_e32 v186, v185, v174
	v_mul_f32_e32 v179, v178, v170
	v_mul_f32_e32 v187, v186, v174
	v_mul_f32_e32 v180, v179, v170
	v_mul_f32_e32 v188, v187, v174
	v_mul_f32_e32 v181, v180, v170
	v_mul_f32_e32 v189, v188, v174
	v_mul_f32_e32 v182, v181, v170
	v_mul_f32_e32 v190, v189, v174
	v_min_f32_e32 v160, v175, v183
	v_mul_f32_e32 v144, v34, v160
	v_min_f32_e32 v162, v179, v187
	v_mul_f32_e32 v34, v50, v162
	v_mul_f32_e32 v164, v175, v167
	v_mul_f32_e32 v165, v183, v171
	v_min_f32_e32 v164, v164, v165
	v_mul_f32_e32 v50, v35, v164
	v_mul_f32_e32 v160, v179, v167
	v_mul_f32_e32 v161, v187, v171
	v_min_f32_e32 v160, v160, v161
	v_mul_f32_e32 v35, v51, v160
	v_mul_f32_e32 v162, v175, v168
	v_mul_f32_e32 v163, v183, v172
	v_min_f32_e32 v162, v162, v163
	v_mul_f32_e32 v51, v36, v162
	v_mul_f32_e32 v164, v179, v168
	v_mul_f32_e32 v165, v187, v172
	v_min_f32_e32 v164, v164, v165
	v_mul_f32_e32 v36, v52, v164
	v_mul_f32_e32 v160, v175, v169
	v_mul_f32_e32 v161, v183, v173
	v_min_f32_e32 v160, v160, v161
	v_mul_f32_e32 v52, v37, v160
	v_mul_f32_e32 v162, v179, v169
	v_mul_f32_e32 v163, v187, v173
	v_min_f32_e32 v162, v162, v163
	v_mul_f32_e32 v37, v53, v162
	v_min_f32_e32 v164, v176, v184
	v_mul_f32_e32 v53, v38, v164
	v_min_f32_e32 v160, v180, v188
	v_mul_f32_e32 v38, v54, v160
	v_mul_f32_e32 v162, v176, v167
	v_mul_f32_e32 v163, v184, v171
	v_min_f32_e32 v162, v162, v163
	v_mul_f32_e32 v54, v39, v162
	v_mul_f32_e32 v164, v180, v167
	v_mul_f32_e32 v165, v188, v171
	v_min_f32_e32 v164, v164, v165
	v_mul_f32_e32 v39, v55, v164
	v_mul_f32_e32 v160, v176, v168
	v_mul_f32_e32 v161, v184, v172
	v_min_f32_e32 v160, v160, v161
	v_mul_f32_e32 v55, v40, v160
	v_mul_f32_e32 v162, v180, v168
	v_mul_f32_e32 v163, v188, v172
	v_min_f32_e32 v162, v162, v163
	v_mul_f32_e32 v40, v56, v162
	v_mul_f32_e32 v164, v176, v169
	v_mul_f32_e32 v165, v184, v173
	v_min_f32_e32 v164, v164, v165
	v_mul_f32_e32 v56, v41, v164
	v_mul_f32_e32 v160, v180, v169
	v_mul_f32_e32 v161, v188, v173
	v_min_f32_e32 v160, v160, v161
	v_mul_f32_e32 v41, v57, v160
	v_min_f32_e32 v162, v177, v185
	v_mul_f32_e32 v57, v42, v162
	v_min_f32_e32 v164, v181, v189
	v_mul_f32_e32 v42, v58, v164
	v_mul_f32_e32 v160, v177, v167
	v_mul_f32_e32 v161, v185, v171
	v_min_f32_e32 v160, v160, v161
	v_mul_f32_e32 v43, v43, v160
	v_mul_f32_e32 v162, v181, v167
	v_mul_f32_e32 v163, v189, v171
	v_min_f32_e32 v162, v162, v163
	v_mul_f32_e32 v58, v59, v162
	v_mul_f32_e32 v164, v177, v168
	v_mul_f32_e32 v165, v185, v172
	v_min_f32_e32 v164, v164, v165
	v_mul_f32_e32 v59, v44, v164
	v_mul_f32_e32 v160, v181, v168
	v_mul_f32_e32 v161, v189, v172
	v_min_f32_e32 v160, v160, v161
	v_mul_f32_e32 v60, v60, v160
	v_mul_f32_e32 v162, v177, v169
	v_mul_f32_e32 v163, v185, v173
	v_min_f32_e32 v162, v162, v163
	v_mul_f32_e32 v147, v45, v162
	v_mul_f32_e32 v164, v181, v169
	v_mul_f32_e32 v165, v189, v173
	v_min_f32_e32 v164, v164, v165
	v_mul_f32_e32 v61, v61, v164
	v_min_f32_e32 v160, v178, v186
	v_mul_f32_e32 v146, v46, v160
	v_min_f32_e32 v162, v182, v190
	v_mul_f32_e32 v62, v62, v162
	v_mul_f32_e32 v164, v178, v167
	v_mul_f32_e32 v165, v186, v171
	v_min_f32_e32 v164, v164, v165
	v_mul_f32_e32 v148, v47, v164
	v_mul_f32_e32 v160, v182, v167
	v_mul_f32_e32 v161, v190, v171
	v_min_f32_e32 v160, v160, v161
	v_mul_f32_e32 v63, v63, v160
	v_mul_f32_e32 v162, v178, v168
	v_mul_f32_e32 v163, v186, v172
	v_min_f32_e32 v162, v162, v163
	v_mul_f32_e32 v149, v48, v162
	v_mul_f32_e32 v164, v182, v168
	v_mul_f32_e32 v165, v190, v172
	v_min_f32_e32 v164, v164, v165
	v_mul_f32_e32 v64, v64, v164
	v_mul_f32_e32 v160, v178, v169
	v_mul_f32_e32 v161, v186, v173
	v_min_f32_e32 v160, v160, v161
	v_mul_f32_e32 v145, v49, v160
	v_mul_f32_e32 v162, v182, v169
	v_mul_f32_e32 v163, v190, v173
	v_min_f32_e32 v162, v162, v163
	v_mul_f32_e32 v65, v65, v162
	v_cvt_pk_bf16_f32 v44, v144, v50
	v_cvt_pk_bf16_f32 v45, v51, v52
	v_cvt_pk_bf16_f32 v46, v53, v54
	v_cvt_pk_bf16_f32 v47, v55, v56
	v_cvt_pk_bf16_f32 v48, v57, v43
	v_cvt_pk_bf16_f32 v49, v59, v147
	v_cvt_pk_bf16_f32 v50, v146, v148
	v_cvt_pk_bf16_f32 v51, v149, v145
	v_cvt_pk_bf16_f32 v34, v34, v35
	v_cvt_pk_bf16_f32 v35, v36, v37
	v_cvt_pk_bf16_f32 v36, v38, v39
	v_cvt_pk_bf16_f32 v37, v40, v41
	v_cvt_pk_bf16_f32 v38, v42, v58
	v_cvt_pk_bf16_f32 v39, v60, v61
	v_cvt_pk_bf16_f32 v40, v62, v63
	v_cvt_pk_bf16_f32 v41, v64, v65
	v_lshl_add_u32 v42, s10, 13, v110
	ds_read_b64_tr_b16 v[52:53], v42 offset:0
	ds_read_b64_tr_b16 v[54:55], v42 offset:0x400
	ds_read_b64_tr_b16 v[56:57], v42 offset:0x800
	ds_read_b64_tr_b16 v[58:59], v42 offset:0xc00
	ds_read_b64_tr_b16 v[60:61], v42 offset:0x1000
	ds_read_b64_tr_b16 v[62:63], v42 offset:0x1400
	ds_read_b64_tr_b16 v[144:145], v42 offset:0x1800
	ds_read_b64_tr_b16 v[146:147], v42 offset:0x1c00
	s_waitcnt lgkmcnt(0)
	v_permlane32_swap_b32_e32 v44, v46
	v_permlane32_swap_b32_e32 v45, v47
	v_permlane32_swap_b32_e32 v48, v50
	v_permlane32_swap_b32_e32 v49, v51
	v_permlane32_swap_b32_e32 v34, v36
	v_permlane32_swap_b32_e32 v35, v37
	v_permlane32_swap_b32_e32 v38, v40
	v_permlane32_swap_b32_e32 v39, v41
	v_mfma_f32_32x32x16_bf16 v[18:33], v[52:55], v[44:47], v[18:33]
	ds_read_b64_tr_b16 v[52:53], v42 offset:0x200
	ds_read_b64_tr_b16 v[54:55], v42 offset:0x600
	v_mfma_f32_32x32x16_bf16 v[18:33], v[56:59], v[48:51], v[18:33]
	ds_read_b64_tr_b16 v[56:57], v42 offset:0xa00
	ds_read_b64_tr_b16 v[58:59], v42 offset:0xe00
	v_mfma_f32_32x32x16_bf16 v[18:33], v[60:63], v[34:37], v[18:33]
	ds_read_b64_tr_b16 v[60:61], v42 offset:0x1200
	ds_read_b64_tr_b16 v[62:63], v42 offset:0x1600
	v_mfma_f32_32x32x16_bf16 v[18:33], v[144:147], v[38:41], v[18:33]
	ds_read_b64_tr_b16 v[144:145], v42 offset:0x1a00
	ds_read_b64_tr_b16 v[146:147], v42 offset:0x1e00
	s_waitcnt lgkmcnt(0)
	v_mfma_f32_32x32x16_bf16 v[2:17], v[52:55], v[44:47], v[2:17]
	s_mov_b64 s[4:5], 0
	s_and_b64 vcc, exec, vcc
	s_mov_b32 s10, 1
	v_mfma_f32_32x32x16_bf16 v[2:17], v[56:59], v[48:51], v[2:17]
	v_mfma_f32_32x32x16_bf16 v[2:17], v[60:63], v[34:37], v[2:17]
	v_mfma_f32_32x32x16_bf16 v[2:17], v[144:147], v[38:41], v[2:17]
	s_cbranch_vccz .LBB0_556
	v_mul_f32_e32 v34, v101, v111
	v_exp_f32_e32 v50, v34
	v_mul_f32_e32 v34, v103, v112
	v_exp_f32_e32 v51, v34
	v_lshlrev_b32_e32 v35, 16, v78
	v_and_b32_e32 v36, 0xffff0000, v78
	v_mul_f32_e32 v34, v50, v35
	v_mul_f32_e32 v37, v50, v36
	v_mul_f32_e32 v36, v51, v36
	v_cvt_pk_bf16_f32 v34, v34, v37
	v_mul_f32_e32 v35, v51, v35
	v_cvt_pk_bf16_f32 v38, v35, v36
	v_lshlrev_b32_e32 v36, 16, v79
	v_and_b32_e32 v37, 0xffff0000, v79
	v_mul_f32_e32 v35, v50, v36
	v_mul_f32_e32 v39, v50, v37
	v_mul_f32_e32 v37, v51, v37
	v_cvt_pk_bf16_f32 v35, v35, v39
	v_mul_f32_e32 v36, v51, v36
	v_cvt_pk_bf16_f32 v39, v36, v37
	v_lshlrev_b32_e32 v37, 16, v80
	v_and_b32_e32 v40, 0xffff0000, v80
	v_mul_f32_e32 v36, v50, v37
	v_mul_f32_e32 v41, v50, v40
	v_cvt_pk_bf16_f32 v36, v36, v41
	v_mul_f32_e32 v37, v51, v37
	v_mul_f32_e32 v40, v51, v40
	v_lshlrev_b32_e32 v41, 16, v81
	v_and_b32_e32 v42, 0xffff0000, v81
	v_cvt_pk_bf16_f32 v40, v37, v40
	v_mul_f32_e32 v37, v50, v41
	v_mul_f32_e32 v43, v50, v42
	v_mul_f32_e32 v41, v51, v41
	v_mul_f32_e32 v42, v51, v42
	v_cvt_pk_bf16_f32 v37, v37, v43
	v_cvt_pk_bf16_f32 v41, v41, v42
	ds_read_b128 v[42:45], v134 offset:32768
	ds_read_b128 v[46:49], v134 offset:40960
	s_waitcnt lgkmcnt(1)
	v_mfma_f32_32x32x16_bf16 v[18:33], v[42:45], v[34:37], v[18:33]
	s_mov_b64 s[4:5], 0x1400
	s_waitcnt lgkmcnt(0)
	v_mfma_f32_32x32x16_bf16 v[18:33], v[46:49], v[38:41], v[18:33]
	ds_read_b128 v[42:45], v134 offset:36864
	ds_read_b128 v[46:49], v134 offset:45056
	s_waitcnt lgkmcnt(1)
	v_mfma_f32_32x32x16_bf16 v[2:17], v[42:45], v[34:37], v[2:17]
	v_lshlrev_b32_e32 v35, 16, v74
	v_and_b32_e32 v36, 0xffff0000, v74
	v_mul_f32_e32 v34, v50, v35
	v_mul_f32_e32 v37, v50, v36
	v_mul_f32_e32 v36, v51, v36
	v_cvt_pk_bf16_f32 v34, v34, v37
	v_mul_f32_e32 v35, v51, v35
	s_waitcnt lgkmcnt(0)
	v_mfma_f32_32x32x16_bf16 v[2:17], v[46:49], v[38:41], v[2:17]
	v_cvt_pk_bf16_f32 v38, v35, v36
	v_lshlrev_b32_e32 v36, 16, v75
	v_and_b32_e32 v37, 0xffff0000, v75
	v_mul_f32_e32 v35, v50, v36
	v_mul_f32_e32 v39, v50, v37
	v_mul_f32_e32 v37, v51, v37
	v_cvt_pk_bf16_f32 v35, v35, v39
	v_mul_f32_e32 v36, v51, v36
	v_cvt_pk_bf16_f32 v39, v36, v37
	v_lshlrev_b32_e32 v37, 16, v76
	v_and_b32_e32 v40, 0xffff0000, v76
	v_mul_f32_e32 v36, v50, v37
	v_mul_f32_e32 v41, v50, v40
	v_cvt_pk_bf16_f32 v36, v36, v41
	v_mul_f32_e32 v37, v51, v37
	v_mul_f32_e32 v40, v51, v40
	v_lshlrev_b32_e32 v41, 16, v77
	v_and_b32_e32 v42, 0xffff0000, v77
	v_cvt_pk_bf16_f32 v40, v37, v40
	v_mul_f32_e32 v37, v50, v41
	v_mul_f32_e32 v43, v50, v42
	v_mul_f32_e32 v41, v51, v41
	v_mul_f32_e32 v42, v51, v42
	v_cvt_pk_bf16_f32 v37, v37, v43
	v_cvt_pk_bf16_f32 v41, v41, v42
	ds_read_b128 v[42:45], v135 offset:32768
	ds_read_b128 v[46:49], v135 offset:40960
	s_waitcnt lgkmcnt(1)
	v_mfma_f32_32x32x16_bf16 v[18:33], v[42:45], v[34:37], v[18:33]
	s_waitcnt lgkmcnt(0)
	v_mfma_f32_32x32x16_bf16 v[18:33], v[46:49], v[38:41], v[18:33]
	ds_read_b128 v[42:45], v135 offset:36864
	ds_read_b128 v[46:49], v135 offset:45056
	s_waitcnt lgkmcnt(1)
	v_mfma_f32_32x32x16_bf16 v[2:17], v[42:45], v[34:37], v[2:17]
	v_lshlrev_b32_e32 v35, 16, v70
	v_and_b32_e32 v36, 0xffff0000, v70
	v_mul_f32_e32 v34, v50, v35
	v_mul_f32_e32 v37, v50, v36
	v_mul_f32_e32 v36, v51, v36
	v_cvt_pk_bf16_f32 v34, v34, v37
	v_mul_f32_e32 v35, v51, v35
	s_waitcnt lgkmcnt(0)
	v_mfma_f32_32x32x16_bf16 v[2:17], v[46:49], v[38:41], v[2:17]
	v_cvt_pk_bf16_f32 v38, v35, v36
	v_lshlrev_b32_e32 v36, 16, v71
	v_and_b32_e32 v37, 0xffff0000, v71
	v_mul_f32_e32 v35, v50, v36
	v_mul_f32_e32 v39, v50, v37
	v_mul_f32_e32 v37, v51, v37
	v_cvt_pk_bf16_f32 v35, v35, v39
	v_mul_f32_e32 v36, v51, v36
	v_cvt_pk_bf16_f32 v39, v36, v37
	v_lshlrev_b32_e32 v37, 16, v72
	v_and_b32_e32 v40, 0xffff0000, v72
	v_mul_f32_e32 v36, v50, v37
	v_mul_f32_e32 v41, v50, v40
	v_cvt_pk_bf16_f32 v36, v36, v41
	v_mul_f32_e32 v37, v51, v37
	v_mul_f32_e32 v40, v51, v40
	v_lshlrev_b32_e32 v41, 16, v73
	v_and_b32_e32 v42, 0xffff0000, v73
	v_cvt_pk_bf16_f32 v40, v37, v40
	v_mul_f32_e32 v37, v50, v41
	v_mul_f32_e32 v43, v50, v42
	v_mul_f32_e32 v41, v51, v41
	v_mul_f32_e32 v42, v51, v42
	v_cvt_pk_bf16_f32 v37, v37, v43
	v_cvt_pk_bf16_f32 v41, v41, v42
	ds_read_b128 v[42:45], v136 offset:32768
	ds_read_b128 v[46:49], v136 offset:40960
	s_waitcnt lgkmcnt(1)
	v_mfma_f32_32x32x16_bf16 v[18:33], v[42:45], v[34:37], v[18:33]
	s_waitcnt lgkmcnt(0)
	v_mfma_f32_32x32x16_bf16 v[18:33], v[46:49], v[38:41], v[18:33]
	ds_read_b128 v[42:45], v136 offset:36864
	ds_read_b128 v[46:49], v136 offset:45056
	s_waitcnt lgkmcnt(1)
	v_mfma_f32_32x32x16_bf16 v[2:17], v[42:45], v[34:37], v[2:17]
	v_lshlrev_b32_e32 v35, 16, v66
	v_and_b32_e32 v36, 0xffff0000, v66
	v_mul_f32_e32 v34, v50, v35
	v_mul_f32_e32 v37, v50, v36
	v_mul_f32_e32 v36, v51, v36
	v_cvt_pk_bf16_f32 v34, v34, v37
	v_mul_f32_e32 v35, v51, v35
	s_waitcnt lgkmcnt(0)
	v_mfma_f32_32x32x16_bf16 v[2:17], v[46:49], v[38:41], v[2:17]
	v_cvt_pk_bf16_f32 v38, v35, v36
	v_lshlrev_b32_e32 v36, 16, v67
	v_and_b32_e32 v37, 0xffff0000, v67
	v_mul_f32_e32 v35, v50, v36
	v_mul_f32_e32 v39, v50, v37
	v_mul_f32_e32 v37, v51, v37
	v_cvt_pk_bf16_f32 v35, v35, v39
	v_mul_f32_e32 v36, v51, v36
	v_cvt_pk_bf16_f32 v39, v36, v37
	v_lshlrev_b32_e32 v37, 16, v68
	v_and_b32_e32 v40, 0xffff0000, v68
	v_mul_f32_e32 v36, v50, v37
	v_mul_f32_e32 v41, v50, v40
	v_cvt_pk_bf16_f32 v36, v36, v41
	v_mul_f32_e32 v37, v51, v37
	v_mul_f32_e32 v40, v51, v40
	v_lshlrev_b32_e32 v41, 16, v69
	v_and_b32_e32 v42, 0xffff0000, v69
	v_cvt_pk_bf16_f32 v40, v37, v40
	v_mul_f32_e32 v37, v50, v41
	v_mul_f32_e32 v43, v50, v42
	v_mul_f32_e32 v41, v51, v41
	v_mul_f32_e32 v42, v51, v42
	v_cvt_pk_bf16_f32 v37, v37, v43
	v_cvt_pk_bf16_f32 v41, v41, v42
	ds_read_b128 v[42:45], v137 offset:32768
	ds_read_b128 v[46:49], v137 offset:40960
	s_waitcnt lgkmcnt(1)
	v_mfma_f32_32x32x16_bf16 v[18:33], v[42:45], v[34:37], v[18:33]
	s_waitcnt lgkmcnt(0)
	v_mfma_f32_32x32x16_bf16 v[18:33], v[46:49], v[38:41], v[18:33]
	ds_read_b128 v[42:45], v137 offset:36864
	ds_read_b128 v[46:49], v137 offset:45056
	s_waitcnt lgkmcnt(1)
	v_mfma_f32_32x32x16_bf16 v[2:17], v[42:45], v[34:37], v[2:17]
	s_waitcnt lgkmcnt(0)
	v_mfma_f32_32x32x16_bf16 v[2:17], v[46:49], v[38:41], v[2:17]
	s_nop 7
	v_mul_f32_e32 v78, v19, v19
	v_fmac_f32_e32 v78, v18, v18
	v_fmac_f32_e32 v78, v20, v20
	v_fmac_f32_e32 v78, v21, v21
	v_fmac_f32_e32 v78, v22, v22
	v_fmac_f32_e32 v78, v23, v23
	v_fmac_f32_e32 v78, v24, v24
	v_fmac_f32_e32 v78, v25, v25
	v_fmac_f32_e32 v78, v26, v26
	v_fmac_f32_e32 v78, v27, v27
	v_fmac_f32_e32 v78, v28, v28
	v_fmac_f32_e32 v78, v29, v29
	v_fmac_f32_e32 v78, v30, v30
	v_fmac_f32_e32 v78, v31, v31
	v_fmac_f32_e32 v78, v32, v32
	v_fmac_f32_e32 v78, v33, v33
	v_fmac_f32_e32 v78, v2, v2
	v_fmac_f32_e32 v78, v3, v3
	v_fmac_f32_e32 v78, v4, v4
	v_fmac_f32_e32 v78, v5, v5
	v_fmac_f32_e32 v78, v6, v6
	v_fmac_f32_e32 v78, v7, v7
	v_fmac_f32_e32 v78, v8, v8
	v_fmac_f32_e32 v78, v9, v9
	v_fmac_f32_e32 v78, v10, v10
	v_fmac_f32_e32 v78, v11, v11
	v_fmac_f32_e32 v78, v12, v12
	v_fmac_f32_e32 v78, v13, v13
	v_fmac_f32_e32 v78, v14, v14
	v_fmac_f32_e32 v78, v15, v15
	v_pk_mul_f32 v[62:63], v[16:17], v[16:17]
	s_and_b64 vcc, exec, s[20:21]
	v_add_f32_e32 v62, v78, v62
	v_add_f32_e32 v62, v62, v63
	v_mov_b32_e32 v63, v62
	s_nop 1
	v_permlane32_swap_b32_e32 v62, v63
	v_add_f32_e32 v62, v62, v63
	v_fmamk_f32 v62, v62, 0x3c800000, v210
	v_rsq_f32_e32 v78, v62
	v_lshlrev_b64 v[62:63], 10, v[104:105]
	v_lshl_add_u64 v[62:63], s[82:83], 0, v[62:63]
	v_lshl_add_u64 v[62:63], v[62:63], 0, s[22:23]
	v_mul_f32_e32 v78, 0x41800000, v78
	v_lshl_add_u64 v[62:63], v[62:63], 0, v[84:85]
	v_rcp_f32_e32 v152, v78
	s_waitcnt vmcnt(7)
	v_lshlrev_b32_e32 v153, 16, v222
	v_and_b32_e32 v154, 0xffff0000, v222
	v_lshlrev_b32_e32 v155, 16, v223
	v_and_b32_e32 v156, 0xffff0000, v223
	v_mul_f32_e32 v157, 0xbfb8aa3b, v153
	v_mul_f32_e32 v158, 0xbfb8aa3b, v154
	v_mul_f32_e32 v159, 0xbfb8aa3b, v155
	v_mul_f32_e32 v160, 0xbfb8aa3b, v156
	v_exp_f32_e32 v157, v157
	v_exp_f32_e32 v158, v158
	v_exp_f32_e32 v159, v159
	v_exp_f32_e32 v160, v160
	v_mul_f32_e32 v161, v18, v238
	v_mul_f32_e32 v162, v19, v239
	v_mul_f32_e32 v163, v20, v240
	v_mul_f32_e32 v164, v21, v241
	v_fma_f32 v157, v157, v152, v152
	v_fma_f32 v158, v158, v152, v152
	v_fma_f32 v159, v159, v152, v152
	v_fma_f32 v160, v160, v152, v152
	v_rcp_f32_e32 v157, v157
	v_rcp_f32_e32 v158, v158
	v_rcp_f32_e32 v159, v159
	v_rcp_f32_e32 v160, v160
	v_mul_f32_e32 v153, v153, v157
	v_mul_f32_e32 v154, v154, v158
	v_mul_f32_e32 v155, v155, v159
	v_mul_f32_e32 v156, v156, v160
	v_mul_f32_e32 v161, v161, v153
	v_mul_f32_e32 v162, v162, v154
	v_mul_f32_e32 v163, v163, v155
	v_mul_f32_e32 v164, v164, v156
	v_cvt_pk_fp8_f32 v18, v161, v162
	v_cvt_pk_fp8_f32 v18, v163, v164 op_sel:[0,0,1]
	s_waitcnt vmcnt(6)
	v_lshlrev_b32_e32 v165, 16, v224
	v_and_b32_e32 v166, 0xffff0000, v224
	v_lshlrev_b32_e32 v167, 16, v225
	v_and_b32_e32 v168, 0xffff0000, v225
	v_mul_f32_e32 v169, 0xbfb8aa3b, v165
	v_mul_f32_e32 v170, 0xbfb8aa3b, v166
	v_mul_f32_e32 v171, 0xbfb8aa3b, v167
	v_mul_f32_e32 v172, 0xbfb8aa3b, v168
	v_exp_f32_e32 v169, v169
	v_exp_f32_e32 v170, v170
	v_exp_f32_e32 v171, v171
	v_exp_f32_e32 v172, v172
	v_mul_f32_e32 v173, v22, v242
	v_mul_f32_e32 v174, v23, v243
	v_mul_f32_e32 v175, v24, v244
	v_mul_f32_e32 v176, v25, v245
	v_fma_f32 v169, v169, v152, v152
	v_fma_f32 v170, v170, v152, v152
	v_fma_f32 v171, v171, v152, v152
	v_fma_f32 v172, v172, v152, v152
	v_rcp_f32_e32 v169, v169
	v_rcp_f32_e32 v170, v170
	v_rcp_f32_e32 v171, v171
	v_rcp_f32_e32 v172, v172
	v_mul_f32_e32 v165, v165, v169
	v_mul_f32_e32 v166, v166, v170
	v_mul_f32_e32 v167, v167, v171
	v_mul_f32_e32 v168, v168, v172
	v_mul_f32_e32 v173, v173, v165
	v_mul_f32_e32 v174, v174, v166
	v_mul_f32_e32 v175, v175, v167
	v_mul_f32_e32 v176, v176, v168
	v_cvt_pk_fp8_f32 v20, v173, v174
	v_cvt_pk_fp8_f32 v20, v175, v176 op_sel:[0,0,1]
	s_waitcnt vmcnt(5)
	v_lshlrev_b32_e32 v153, 16, v226
	v_and_b32_e32 v154, 0xffff0000, v226
	v_lshlrev_b32_e32 v155, 16, v227
	v_and_b32_e32 v156, 0xffff0000, v227
	v_mul_f32_e32 v157, 0xbfb8aa3b, v153
	v_mul_f32_e32 v158, 0xbfb8aa3b, v154
	v_mul_f32_e32 v159, 0xbfb8aa3b, v155
	v_mul_f32_e32 v160, 0xbfb8aa3b, v156
	v_exp_f32_e32 v157, v157
	v_exp_f32_e32 v158, v158
	v_exp_f32_e32 v159, v159
	v_exp_f32_e32 v160, v160
	v_mul_f32_e32 v161, v26, v246
	v_mul_f32_e32 v162, v27, v247
	v_mul_f32_e32 v163, v28, v248
	v_mul_f32_e32 v164, v29, v249
	v_fma_f32 v157, v157, v152, v152
	v_fma_f32 v158, v158, v152, v152
	v_fma_f32 v159, v159, v152, v152
	v_fma_f32 v160, v160, v152, v152
	v_rcp_f32_e32 v157, v157
	v_rcp_f32_e32 v158, v158
	v_rcp_f32_e32 v159, v159
	v_rcp_f32_e32 v160, v160
	v_mul_f32_e32 v153, v153, v157
	v_mul_f32_e32 v154, v154, v158
	v_mul_f32_e32 v155, v155, v159
	v_mul_f32_e32 v156, v156, v160
	v_mul_f32_e32 v161, v161, v153
	v_mul_f32_e32 v162, v162, v154
	v_mul_f32_e32 v163, v163, v155
	v_mul_f32_e32 v164, v164, v156
	v_cvt_pk_fp8_f32 v19, v161, v162
	v_cvt_pk_fp8_f32 v19, v163, v164 op_sel:[0,0,1]
	s_waitcnt vmcnt(4)
	v_lshlrev_b32_e32 v165, 16, v228
	v_and_b32_e32 v166, 0xffff0000, v228
	v_lshlrev_b32_e32 v167, 16, v229
	v_and_b32_e32 v168, 0xffff0000, v229
	v_mul_f32_e32 v169, 0xbfb8aa3b, v165
	v_mul_f32_e32 v170, 0xbfb8aa3b, v166
	v_mul_f32_e32 v171, 0xbfb8aa3b, v167
	v_mul_f32_e32 v172, 0xbfb8aa3b, v168
	v_exp_f32_e32 v169, v169
	v_exp_f32_e32 v170, v170
	v_exp_f32_e32 v171, v171
	v_exp_f32_e32 v172, v172
	v_mul_f32_e32 v173, v30, v250
	v_mul_f32_e32 v174, v31, v251
	v_mul_f32_e32 v175, v32, v252
	v_mul_f32_e32 v176, v33, v253
	v_fma_f32 v169, v169, v152, v152
	v_fma_f32 v170, v170, v152, v152
	v_fma_f32 v171, v171, v152, v152
	v_fma_f32 v172, v172, v152, v152
	v_rcp_f32_e32 v169, v169
	v_rcp_f32_e32 v170, v170
	v_rcp_f32_e32 v171, v171
	v_rcp_f32_e32 v172, v172
	v_mul_f32_e32 v165, v165, v169
	v_mul_f32_e32 v166, v166, v170
	v_mul_f32_e32 v167, v167, v171
	v_mul_f32_e32 v168, v168, v172
	v_mul_f32_e32 v173, v173, v165
	v_mul_f32_e32 v174, v174, v166
	v_mul_f32_e32 v175, v175, v167
	v_mul_f32_e32 v176, v176, v168
	v_cvt_pk_fp8_f32 v21, v173, v174
	v_cvt_pk_fp8_f32 v21, v175, v176 op_sel:[0,0,1]
	v_permlane32_swap_b32_e32 v18, v19
	s_nop 0
	v_permlane32_swap_b32_e32 v20, v21
	global_store_dwordx4 v[62:63], v[18:21], off offset:768
	s_waitcnt vmcnt(4)
	v_lshlrev_b32_e32 v153, 16, v230
	v_and_b32_e32 v154, 0xffff0000, v230
	v_lshlrev_b32_e32 v155, 16, v231
	v_and_b32_e32 v156, 0xffff0000, v231
	v_mul_f32_e32 v157, 0xbfb8aa3b, v153
	v_mul_f32_e32 v158, 0xbfb8aa3b, v154
	v_mul_f32_e32 v159, 0xbfb8aa3b, v155
	v_mul_f32_e32 v160, 0xbfb8aa3b, v156
	v_exp_f32_e32 v157, v157
	v_exp_f32_e32 v158, v158
	v_exp_f32_e32 v159, v159
	v_exp_f32_e32 v160, v160
	v_mul_f32_e32 v161, v2, v200
	v_mul_f32_e32 v162, v3, v201
	v_mul_f32_e32 v163, v4, v202
	v_mul_f32_e32 v164, v5, v203
	v_fma_f32 v157, v157, v152, v152
	v_fma_f32 v158, v158, v152, v152
	v_fma_f32 v159, v159, v152, v152
	v_fma_f32 v160, v160, v152, v152
	v_rcp_f32_e32 v157, v157
	v_rcp_f32_e32 v158, v158
	v_rcp_f32_e32 v159, v159
	v_rcp_f32_e32 v160, v160
	v_mul_f32_e32 v153, v153, v157
	v_mul_f32_e32 v154, v154, v158
	v_mul_f32_e32 v155, v155, v159
	v_mul_f32_e32 v156, v156, v160
	v_mul_f32_e32 v161, v161, v153
	v_mul_f32_e32 v162, v162, v154
	v_mul_f32_e32 v163, v163, v155
	v_mul_f32_e32 v164, v164, v156
	v_cvt_pk_fp8_f32 v2, v161, v162
	v_cvt_pk_fp8_f32 v2, v163, v164 op_sel:[0,0,1]
	s_waitcnt vmcnt(3)
	v_lshlrev_b32_e32 v165, 16, v232
	v_and_b32_e32 v166, 0xffff0000, v232
	v_lshlrev_b32_e32 v167, 16, v233
	v_and_b32_e32 v168, 0xffff0000, v233
	v_mul_f32_e32 v169, 0xbfb8aa3b, v165
	v_mul_f32_e32 v170, 0xbfb8aa3b, v166
	v_mul_f32_e32 v171, 0xbfb8aa3b, v167
	v_mul_f32_e32 v172, 0xbfb8aa3b, v168
	v_exp_f32_e32 v169, v169
	v_exp_f32_e32 v170, v170
	v_exp_f32_e32 v171, v171
	v_exp_f32_e32 v172, v172
	v_mul_f32_e32 v173, v6, v204
	v_mul_f32_e32 v174, v7, v205
	v_mul_f32_e32 v175, v8, v206
	v_mul_f32_e32 v176, v9, v207
	v_fma_f32 v169, v169, v152, v152
	v_fma_f32 v170, v170, v152, v152
	v_fma_f32 v171, v171, v152, v152
	v_fma_f32 v172, v172, v152, v152
	v_rcp_f32_e32 v169, v169
	v_rcp_f32_e32 v170, v170
	v_rcp_f32_e32 v171, v171
	v_rcp_f32_e32 v172, v172
	v_mul_f32_e32 v165, v165, v169
	v_mul_f32_e32 v166, v166, v170
	v_mul_f32_e32 v167, v167, v171
	v_mul_f32_e32 v168, v168, v172
	v_mul_f32_e32 v173, v173, v165
	v_mul_f32_e32 v174, v174, v166
	v_mul_f32_e32 v175, v175, v167
	v_mul_f32_e32 v176, v176, v168
	v_cvt_pk_fp8_f32 v4, v173, v174
	v_cvt_pk_fp8_f32 v4, v175, v176 op_sel:[0,0,1]
	s_waitcnt vmcnt(2)
	v_lshlrev_b32_e32 v153, 16, v234
	v_and_b32_e32 v154, 0xffff0000, v234
	v_lshlrev_b32_e32 v155, 16, v235
	v_and_b32_e32 v156, 0xffff0000, v235
	v_mul_f32_e32 v157, 0xbfb8aa3b, v153
	v_mul_f32_e32 v158, 0xbfb8aa3b, v154
	v_mul_f32_e32 v159, 0xbfb8aa3b, v155
	v_mul_f32_e32 v160, 0xbfb8aa3b, v156
	v_exp_f32_e32 v157, v157
	v_exp_f32_e32 v158, v158
	v_exp_f32_e32 v159, v159
	v_exp_f32_e32 v160, v160
	v_mul_f32_e32 v161, v10, v214
	v_mul_f32_e32 v162, v11, v215
	v_mul_f32_e32 v163, v12, v216
	v_mul_f32_e32 v164, v13, v217
	v_fma_f32 v157, v157, v152, v152
	v_fma_f32 v158, v158, v152, v152
	v_fma_f32 v159, v159, v152, v152
	v_fma_f32 v160, v160, v152, v152
	v_rcp_f32_e32 v157, v157
	v_rcp_f32_e32 v158, v158
	v_rcp_f32_e32 v159, v159
	v_rcp_f32_e32 v160, v160
	v_mul_f32_e32 v153, v153, v157
	v_mul_f32_e32 v154, v154, v158
	v_mul_f32_e32 v155, v155, v159
	v_mul_f32_e32 v156, v156, v160
	v_mul_f32_e32 v161, v161, v153
	v_mul_f32_e32 v162, v162, v154
	v_mul_f32_e32 v163, v163, v155
	v_mul_f32_e32 v164, v164, v156
	v_cvt_pk_fp8_f32 v3, v161, v162
	v_cvt_pk_fp8_f32 v3, v163, v164 op_sel:[0,0,1]
	s_waitcnt vmcnt(1)
	v_lshlrev_b32_e32 v165, 16, v236
	v_and_b32_e32 v166, 0xffff0000, v236
	v_lshlrev_b32_e32 v167, 16, v237
	v_and_b32_e32 v168, 0xffff0000, v237
	v_mul_f32_e32 v169, 0xbfb8aa3b, v165
	v_mul_f32_e32 v170, 0xbfb8aa3b, v166
	v_mul_f32_e32 v171, 0xbfb8aa3b, v167
	v_mul_f32_e32 v172, 0xbfb8aa3b, v168
	v_exp_f32_e32 v169, v169
	v_exp_f32_e32 v170, v170
	v_exp_f32_e32 v171, v171
	v_exp_f32_e32 v172, v172
	v_mul_f32_e32 v173, v14, v192
	v_mul_f32_e32 v174, v15, v193
	v_mul_f32_e32 v175, v16, v194
	v_mul_f32_e32 v176, v17, v195
	v_fma_f32 v169, v169, v152, v152
	v_fma_f32 v170, v170, v152, v152
	v_fma_f32 v171, v171, v152, v152
	v_fma_f32 v172, v172, v152, v152
	v_rcp_f32_e32 v169, v169
	v_rcp_f32_e32 v170, v170
	v_rcp_f32_e32 v171, v171
	v_rcp_f32_e32 v172, v172
	v_mul_f32_e32 v165, v165, v169
	v_mul_f32_e32 v166, v166, v170
	v_mul_f32_e32 v167, v167, v171
	v_mul_f32_e32 v168, v168, v172
	v_mul_f32_e32 v173, v173, v165
	v_mul_f32_e32 v174, v174, v166
	v_mul_f32_e32 v175, v175, v167
	v_mul_f32_e32 v176, v176, v168
	v_cvt_pk_fp8_f32 v5, v173, v174
	v_cvt_pk_fp8_f32 v5, v175, v176 op_sel:[0,0,1]
	v_permlane32_swap_b32_e32 v2, v3
	s_nop 0
	v_permlane32_swap_b32_e32 v4, v5
	global_store_dwordx4 v[62:63], v[2:5], off offset:800
	s_cbranch_vccz .LBB0_550
	s_waitcnt vmcnt(0)
	s_barrier
	s_and_saveexec_b64 s[4:5], s[0:1]
	s_cbranch_execz .LBB0_549
	s_mov_b64 s[10:11], exec
	v_mbcnt_lo_u32_b32 v2, s10, 0
	buffer_wbl2 sc1
	s_waitcnt vmcnt(0)
	s_waitcnt vmcnt(0)
	v_mbcnt_hi_u32_b32 v2, s11, v2
	v_cmp_eq_u32_e32 vcc, 0, v2
	s_and_b64 s[14:15], exec, vcc
	s_mov_b64 exec, s[14:15]
	s_cbranch_execz .LBB0_549
	s_bcnt1_i32_b64 s10, s[10:11]
	v_mov_b32_e32 v2, s10
	global_atomic_add v0, v2, s[84:85]
	s_branch .LBB0_549
